# back-edge rotation in all four GEMM K-loops: per-iteration address SALU block moved ahead of the loop-back barrier
# baseline (speedup 1.0000x reference)
.LBB3_32:
	v_mov_b32_e32 v47, 0
	s_andn2_b64 vcc, exec, s[18:19]
	v_mov_b32_e32 v46, v47
	v_mov_b32_e32 v45, v47
	v_mov_b32_e32 v44, v47
	v_mov_b32_e32 v43, v47
	v_mov_b32_e32 v42, v47
	v_mov_b32_e32 v41, v47
	v_mov_b32_e32 v40, v47
	v_mov_b32_e32 v39, v47
	v_mov_b32_e32 v38, v47
	v_mov_b32_e32 v37, v47
	v_mov_b32_e32 v36, v47
	v_mov_b32_e32 v35, v47
	v_mov_b32_e32 v34, v47
	v_mov_b32_e32 v33, v47
	v_mov_b32_e32 v32, v47
	v_mov_b32_e32 v31, v47
	v_mov_b32_e32 v30, v47
	v_mov_b32_e32 v29, v47
	v_mov_b32_e32 v28, v47
	v_mov_b32_e32 v27, v47
	v_mov_b32_e32 v26, v47
	v_mov_b32_e32 v25, v47
	v_mov_b32_e32 v24, v47
	v_mov_b32_e32 v23, v47
	v_mov_b32_e32 v22, v47
	v_mov_b32_e32 v21, v47
	v_mov_b32_e32 v20, v47
	v_mov_b32_e32 v19, v47
	v_mov_b32_e32 v18, v47
	v_mov_b32_e32 v17, v47
	v_mov_b32_e32 v16, v47
	v_mov_b32_e32 v15, v47
	v_mov_b32_e32 v14, v47
	v_mov_b32_e32 v13, v47
	v_mov_b32_e32 v12, v47
	v_mov_b32_e32 v11, v47
	v_mov_b32_e32 v10, v47
	v_mov_b32_e32 v9, v47
	v_mov_b32_e32 v8, v47
	v_mov_b32_e32 v7, v47
	v_mov_b32_e32 v6, v47
	v_mov_b32_e32 v5, v47
	v_mov_b32_e32 v4, v47
	v_mov_b32_e32 v3, v47
	v_mov_b32_e32 v2, v47
	v_mov_b32_e32 v1, v47
	v_mov_b32_e32 v0, v47
	s_cbranch_vccnz .LBB3_21
	v_mov_b32_e32 v0, 0
	v_lshl_add_u64 v[72:73], s[20:21], 0, v[60:61]
	v_lshl_add_u64 v[74:75], s[20:21], 0, v[62:63]
	v_lshl_add_u64 v[76:77], s[22:23], 0, v[64:65]
	v_lshl_add_u64 v[78:79], s[22:23], 0, v[66:67]
	v_lshl_add_u64 v[80:81], s[22:23], 0, v[68:69]
	s_mov_b32 s63, 0
	s_mov_b64 s[24:25], 0
	v_mov_b32_e32 v1, v0
	v_mov_b32_e32 v2, v0
	v_mov_b32_e32 v3, v0
	v_mov_b32_e32 v4, v0
	v_mov_b32_e32 v5, v0
	v_mov_b32_e32 v6, v0
	v_mov_b32_e32 v7, v0
	v_mov_b32_e32 v8, v0
	v_mov_b32_e32 v9, v0
	v_mov_b32_e32 v10, v0
	v_mov_b32_e32 v11, v0
	v_mov_b32_e32 v12, v0
	v_mov_b32_e32 v13, v0
	v_mov_b32_e32 v14, v0
	v_mov_b32_e32 v15, v0
	v_mov_b32_e32 v16, v0
	v_mov_b32_e32 v17, v0
	v_mov_b32_e32 v18, v0
	v_mov_b32_e32 v19, v0
	v_mov_b32_e32 v20, v0
	v_mov_b32_e32 v21, v0
	v_mov_b32_e32 v22, v0
	v_mov_b32_e32 v23, v0
	v_mov_b32_e32 v24, v0
	v_mov_b32_e32 v25, v0
	v_mov_b32_e32 v26, v0
	v_mov_b32_e32 v27, v0
	v_mov_b32_e32 v28, v0
	v_mov_b32_e32 v29, v0
	v_mov_b32_e32 v30, v0
	v_mov_b32_e32 v31, v0
	v_mov_b32_e32 v32, v0
	v_mov_b32_e32 v33, v0
	v_mov_b32_e32 v34, v0
	v_mov_b32_e32 v35, v0
	v_mov_b32_e32 v36, v0
	v_mov_b32_e32 v37, v0
	v_mov_b32_e32 v38, v0
	v_mov_b32_e32 v39, v0
	v_mov_b32_e32 v40, v0
	v_mov_b32_e32 v41, v0
	v_mov_b32_e32 v42, v0
	v_mov_b32_e32 v43, v0
	v_mov_b32_e32 v44, v0
	v_mov_b32_e32 v45, v0
	v_mov_b32_e32 v46, v0
	v_mov_b32_e32 v47, v0
	s_add_u32 s26, s20, s24
	s_addc_u32 s27, s21, s25
	s_add_u32 s26, s26, 0x180
	s_addc_u32 s27, s27, 0
	s_add_u32 s64, s22, s24
	s_addc_u32 s65, s23, s25
	s_add_u32 s66, s64, 0x180
	s_addc_u32 s67, s65, 0
	s_cmp_eq_u32 s56, s63
	s_cselect_b32 s65, s5, s27
	s_cselect_b32 s64, s4, s26
	s_cselect_b32 s27, s7, s67
	s_cselect_b32 s26, s6, s66
	s_add_i32 s66, s58, s38
	v_lshl_add_u64 v[146:147], v[72:73], 0, s[24:25]
.LBB3_34:
	s_mov_b32 m0, s66
	ds_read_b128 v[98:101], v94 offset:16384
	ds_read_b128 v[102:105], v94 offset:17408
	ds_read_b128 v[106:109], v94 offset:18432
	ds_read_b128 v[110:113], v94 offset:19456
	ds_read_b128 v[114:117], v95
	ds_read_b128 v[118:121], v95 offset:1024
	ds_read_b128 v[122:125], v95 offset:2048
	ds_read_b128 v[126:129], v95 offset:3072
	ds_read_b128 v[130:133], v95 offset:4096
	ds_read_b128 v[134:137], v95 offset:5120
	ds_read_b128 v[138:141], v95 offset:6144
	ds_read_b128 v[142:145], v95 offset:7168
	global_load_lds_dwordx4 v[146:147], off
	v_lshl_add_u64 v[146:147], v[74:75], 0, s[24:25]
	s_add_i32 m0, s66, 0x2000
	s_nop 0
	global_load_lds_dwordx4 v[146:147], off
	s_barrier
	s_waitcnt lgkmcnt(0)
	s_setprio 1
	s_waitcnt lgkmcnt(0)
	v_mfma_f32_16x16x32_f16 v[44:47], v[98:101], v[114:117], v[44:47]
	v_mfma_f32_16x16x32_f16 v[40:43], v[106:109], v[114:117], v[40:43]
	v_mfma_f32_16x16x32_f16 v[32:35], v[98:101], v[122:125], v[32:35]
	v_mfma_f32_16x16x32_f16 v[28:31], v[106:109], v[122:125], v[28:31]
	v_mfma_f32_16x16x32_f16 v[20:23], v[98:101], v[130:133], v[20:23]
	v_mfma_f32_16x16x32_f16 v[16:19], v[106:109], v[130:133], v[16:19]
	v_mfma_f32_16x16x32_f16 v[8:11], v[98:101], v[138:141], v[8:11]
	v_mfma_f32_16x16x32_f16 v[4:7], v[106:109], v[138:141], v[4:7]
	v_mfma_f32_16x16x32_f16 v[44:47], v[102:105], v[118:121], v[44:47]
	v_mfma_f32_16x16x32_f16 v[40:43], v[110:113], v[118:121], v[40:43]
	v_mfma_f32_16x16x32_f16 v[32:35], v[102:105], v[126:129], v[32:35]
	v_mfma_f32_16x16x32_f16 v[28:31], v[110:113], v[126:129], v[28:31]
	v_mfma_f32_16x16x32_f16 v[20:23], v[102:105], v[134:137], v[20:23]
	v_mfma_f32_16x16x32_f16 v[16:19], v[110:113], v[134:137], v[16:19]
	v_mfma_f32_16x16x32_f16 v[8:11], v[102:105], v[142:145], v[8:11]
	v_mfma_f32_16x16x32_f16 v[4:7], v[110:113], v[142:145], v[4:7]
	s_setprio 0
	s_barrier
	v_lshl_add_u64 v[106:107], v[76:77], 0, s[24:25]
	s_add_i32 m0, s43, 0x18000
	ds_read_b128 v[98:101], v94 offset:20480
	ds_read_b128 v[102:105], v94 offset:21504
	global_load_lds_dwordx4 v[106:107], off
	v_lshl_add_u64 v[106:107], v[78:79], 0, s[24:25]
	s_add_i32 m0, s43, 0x1a000
	s_nop 0
	global_load_lds_dwordx4 v[106:107], off
	v_lshl_add_u64 v[106:107], v[80:81], 0, s[24:25]
	s_add_i32 m0, s43, 0x1c000
	s_nop 0
	global_load_lds_dwordx4 v[106:107], off
	s_waitcnt vmcnt(5)
	s_barrier
	s_waitcnt lgkmcnt(0)
	s_setprio 1
	s_waitcnt lgkmcnt(0)
	v_mfma_f32_16x16x32_f16 v[36:39], v[98:101], v[114:117], v[36:39]
	v_mfma_f32_16x16x32_f16 v[24:27], v[98:101], v[122:125], v[24:27]
	v_mfma_f32_16x16x32_f16 v[12:15], v[98:101], v[130:133], v[12:15]
	v_mfma_f32_16x16x32_f16 v[0:3], v[98:101], v[138:141], v[0:3]
	v_mfma_f32_16x16x32_f16 v[36:39], v[102:105], v[118:121], v[36:39]
	v_mfma_f32_16x16x32_f16 v[24:27], v[102:105], v[126:129], v[24:27]
	v_mfma_f32_16x16x32_f16 v[12:15], v[102:105], v[134:137], v[12:15]
	v_mfma_f32_16x16x32_f16 v[0:3], v[102:105], v[142:145], v[0:3]
	s_setprio 0
	s_barrier
	s_mov_b32 m0, s43
	v_lshl_add_u64 v[146:147], s[64:65], 0, v[48:49]
	ds_read_b128 v[98:101], v94 offset:57344
	ds_read_b128 v[102:105], v94 offset:58368
	ds_read_b128 v[106:109], v94 offset:59392
	ds_read_b128 v[110:113], v94 offset:60416
	ds_read_b128 v[114:117], v95 offset:40960
	ds_read_b128 v[118:121], v95 offset:41984
	ds_read_b128 v[122:125], v95 offset:43008
	ds_read_b128 v[126:129], v95 offset:44032
	ds_read_b128 v[130:133], v95 offset:45056
	ds_read_b128 v[134:137], v95 offset:46080
	ds_read_b128 v[138:141], v95 offset:47104
	ds_read_b128 v[142:145], v95 offset:48128
	global_load_lds_dwordx4 v[146:147], off
	v_lshl_add_u64 v[148:149], s[64:65], 0, v[52:53]
	s_mov_b32 m0, s44
	s_nop 0
	global_load_lds_dwordx4 v[148:149], off
	s_barrier
	s_waitcnt lgkmcnt(0)
	s_setprio 1
	s_waitcnt lgkmcnt(0)
	v_mfma_f32_16x16x32_f16 v[44:47], v[98:101], v[114:117], v[44:47]
	v_mfma_f32_16x16x32_f16 v[40:43], v[106:109], v[114:117], v[40:43]
	v_mfma_f32_16x16x32_f16 v[32:35], v[98:101], v[122:125], v[32:35]
	v_mfma_f32_16x16x32_f16 v[28:31], v[106:109], v[122:125], v[28:31]
	v_mfma_f32_16x16x32_f16 v[20:23], v[98:101], v[130:133], v[20:23]
	v_mfma_f32_16x16x32_f16 v[16:19], v[106:109], v[130:133], v[16:19]
	v_mfma_f32_16x16x32_f16 v[8:11], v[98:101], v[138:141], v[8:11]
	v_mfma_f32_16x16x32_f16 v[4:7], v[106:109], v[138:141], v[4:7]
	v_mfma_f32_16x16x32_f16 v[44:47], v[102:105], v[118:121], v[44:47]
	v_mfma_f32_16x16x32_f16 v[40:43], v[110:113], v[118:121], v[40:43]
	v_mfma_f32_16x16x32_f16 v[32:35], v[102:105], v[126:129], v[32:35]
	v_mfma_f32_16x16x32_f16 v[28:31], v[110:113], v[126:129], v[28:31]
	v_mfma_f32_16x16x32_f16 v[20:23], v[102:105], v[134:137], v[20:23]
	v_mfma_f32_16x16x32_f16 v[16:19], v[110:113], v[134:137], v[16:19]
	v_mfma_f32_16x16x32_f16 v[8:11], v[102:105], v[142:145], v[8:11]
	v_mfma_f32_16x16x32_f16 v[4:7], v[110:113], v[142:145], v[4:7]
	s_setprio 0
	s_barrier
	s_mov_b32 m0, s45
	v_lshl_add_u64 v[150:151], s[26:27], 0, v[50:51]
	ds_read_b128 v[98:101], v94 offset:61440
	ds_read_b128 v[102:105], v94 offset:62464
	global_load_lds_dwordx4 v[150:151], off
	v_lshl_add_u64 v[152:153], s[26:27], 0, v[54:55]
	s_mov_b32 m0, s46
	v_lshl_add_u64 v[154:155], s[26:27], 0, v[56:57]
	global_load_lds_dwordx4 v[152:153], off
	s_mov_b32 m0, s47
	s_nop 0
	global_load_lds_dwordx4 v[154:155], off
	s_waitcnt vmcnt(5)
	s_barrier
	s_waitcnt lgkmcnt(0)
	s_setprio 1
	s_waitcnt lgkmcnt(0)
	v_mfma_f32_16x16x32_f16 v[36:39], v[98:101], v[114:117], v[36:39]
	v_mfma_f32_16x16x32_f16 v[24:27], v[98:101], v[122:125], v[24:27]
	v_mfma_f32_16x16x32_f16 v[12:15], v[98:101], v[130:133], v[12:15]
	v_mfma_f32_16x16x32_f16 v[0:3], v[98:101], v[138:141], v[0:3]
	v_mfma_f32_16x16x32_f16 v[36:39], v[102:105], v[118:121], v[36:39]
	v_mfma_f32_16x16x32_f16 v[24:27], v[102:105], v[126:129], v[24:27]
	v_mfma_f32_16x16x32_f16 v[12:15], v[102:105], v[134:137], v[12:15]
	v_mfma_f32_16x16x32_f16 v[0:3], v[102:105], v[142:145], v[0:3]
	s_setprio 0
	s_barrier
	s_mov_b32 m0, s52
	v_lshl_add_u64 v[146:147], v[146:147], 0, s[16:17]
	ds_read_b128 v[98:101], v96
	ds_read_b128 v[102:105], v96 offset:1024
	ds_read_b128 v[106:109], v96 offset:2048
	ds_read_b128 v[110:113], v96 offset:3072
	ds_read_b128 v[114:117], v97
	ds_read_b128 v[118:121], v97 offset:1024
	ds_read_b128 v[122:125], v97 offset:2048
	ds_read_b128 v[126:129], v97 offset:3072
	ds_read_b128 v[130:133], v97 offset:4096
	ds_read_b128 v[134:137], v97 offset:5120
	ds_read_b128 v[138:141], v97 offset:6144
	ds_read_b128 v[142:145], v97 offset:7168
	global_load_lds_dwordx4 v[146:147], off
	v_lshl_add_u64 v[146:147], v[148:149], 0, s[16:17]
	s_mov_b32 m0, s53
	s_nop 0
	global_load_lds_dwordx4 v[146:147], off
	s_barrier
	s_waitcnt lgkmcnt(0)
	s_setprio 1
	s_waitcnt lgkmcnt(0)
	v_mfma_f32_16x16x32_f16 v[44:47], v[98:101], v[114:117], v[44:47]
	v_mfma_f32_16x16x32_f16 v[40:43], v[106:109], v[114:117], v[40:43]
	v_mfma_f32_16x16x32_f16 v[32:35], v[98:101], v[122:125], v[32:35]
	v_mfma_f32_16x16x32_f16 v[28:31], v[106:109], v[122:125], v[28:31]
	v_mfma_f32_16x16x32_f16 v[20:23], v[98:101], v[130:133], v[20:23]
	v_mfma_f32_16x16x32_f16 v[16:19], v[106:109], v[130:133], v[16:19]
	v_mfma_f32_16x16x32_f16 v[8:11], v[98:101], v[138:141], v[8:11]
	v_mfma_f32_16x16x32_f16 v[4:7], v[106:109], v[138:141], v[4:7]
	v_mfma_f32_16x16x32_f16 v[44:47], v[102:105], v[118:121], v[44:47]
	v_mfma_f32_16x16x32_f16 v[40:43], v[110:113], v[118:121], v[40:43]
	v_mfma_f32_16x16x32_f16 v[32:35], v[102:105], v[126:129], v[32:35]
	v_mfma_f32_16x16x32_f16 v[28:31], v[110:113], v[126:129], v[28:31]
	v_mfma_f32_16x16x32_f16 v[20:23], v[102:105], v[134:137], v[20:23]
	v_mfma_f32_16x16x32_f16 v[16:19], v[110:113], v[134:137], v[16:19]
	v_mfma_f32_16x16x32_f16 v[8:11], v[102:105], v[142:145], v[8:11]
	v_mfma_f32_16x16x32_f16 v[4:7], v[110:113], v[142:145], v[4:7]
	s_setprio 0
	s_barrier
	s_mov_b32 m0, s54
	v_lshl_add_u64 v[106:107], v[150:151], 0, s[16:17]
	ds_read_b128 v[98:101], v96 offset:4096
	ds_read_b128 v[102:105], v96 offset:5120
	global_load_lds_dwordx4 v[106:107], off
	v_lshl_add_u64 v[106:107], v[152:153], 0, s[16:17]
	s_add_i32 m0, s54, 0x2000
	s_nop 0
	global_load_lds_dwordx4 v[106:107], off
	v_lshl_add_u64 v[106:107], v[154:155], 0, s[16:17]
	s_add_i32 m0, s54, 0x4000
	s_nop 0
	global_load_lds_dwordx4 v[106:107], off
	s_waitcnt vmcnt(5)
	s_barrier
	s_waitcnt lgkmcnt(0)
	s_setprio 1
	s_waitcnt lgkmcnt(0)
	v_mfma_f32_16x16x32_f16 v[36:39], v[98:101], v[114:117], v[36:39]
	v_mfma_f32_16x16x32_f16 v[24:27], v[98:101], v[122:125], v[24:27]
	v_mfma_f32_16x16x32_f16 v[12:15], v[98:101], v[130:133], v[12:15]
	v_mfma_f32_16x16x32_f16 v[0:3], v[98:101], v[138:141], v[0:3]
	v_mfma_f32_16x16x32_f16 v[36:39], v[102:105], v[118:121], v[36:39]
	v_mfma_f32_16x16x32_f16 v[24:27], v[102:105], v[126:129], v[24:27]
	v_mfma_f32_16x16x32_f16 v[12:15], v[102:105], v[134:137], v[12:15]
	v_mfma_f32_16x16x32_f16 v[0:3], v[102:105], v[142:145], v[0:3]
	s_setprio 0
	s_add_i32 s63, s63, 3
	s_add_u32 s24, s24, 0x180
	s_addc_u32 s25, s25, 0
	s_cmp_ge_i32 s63, s49
	s_cbranch_scc1 .Lrot_exit_qkv
	s_add_u32 s26, s20, s24
	s_addc_u32 s27, s21, s25
	s_add_u32 s26, s26, 0x180
	s_addc_u32 s27, s27, 0
	s_add_u32 s64, s22, s24
	s_addc_u32 s65, s23, s25
	s_add_u32 s66, s64, 0x180
	s_addc_u32 s67, s65, 0
	s_cmp_eq_u32 s56, s63
	s_cselect_b32 s65, s5, s27
	s_cselect_b32 s64, s4, s26
	s_cselect_b32 s27, s7, s67
	s_cselect_b32 s26, s6, s66
	s_add_i32 s66, s58, s38
	v_lshl_add_u64 v[146:147], v[72:73], 0, s[24:25]
	s_barrier
	s_branch .LBB3_34
.Lrot_exit_qkv:
	s_barrier
	s_branch .LBB3_21

.LBB4_20:
	v_mov_b32_e32 v97, 0
	s_andn2_b64 vcc, exec, s[24:25]
	v_mov_b32_e32 v96, v97
	v_mov_b32_e32 v95, v97
	v_mov_b32_e32 v94, v97
	v_mov_b32_e32 v93, v97
	v_mov_b32_e32 v92, v97
	v_mov_b32_e32 v91, v97
	v_mov_b32_e32 v90, v97
	v_mov_b32_e32 v89, v97
	v_mov_b32_e32 v88, v97
	v_mov_b32_e32 v87, v97
	v_mov_b32_e32 v86, v97
	v_mov_b32_e32 v85, v97
	v_mov_b32_e32 v84, v97
	v_mov_b32_e32 v83, v97
	v_mov_b32_e32 v82, v97
	v_mov_b32_e32 v81, v97
	v_mov_b32_e32 v80, v97
	v_mov_b32_e32 v79, v97
	v_mov_b32_e32 v78, v97
	v_mov_b32_e32 v77, v97
	v_mov_b32_e32 v76, v97
	v_mov_b32_e32 v75, v97
	v_mov_b32_e32 v74, v97
	v_mov_b32_e32 v73, v97
	v_mov_b32_e32 v72, v97
	v_mov_b32_e32 v71, v97
	v_mov_b32_e32 v70, v97
	v_mov_b32_e32 v69, v97
	v_mov_b32_e32 v68, v97
	v_mov_b32_e32 v67, v97
	v_mov_b32_e32 v66, v97
	v_mov_b32_e32 v65, v97
	v_mov_b32_e32 v64, v97
	v_mov_b32_e32 v63, v97
	v_mov_b32_e32 v62, v97
	v_mov_b32_e32 v61, v97
	v_mov_b32_e32 v60, v97
	v_mov_b32_e32 v59, v97
	v_mov_b32_e32 v58, v97
	v_mov_b32_e32 v57, v97
	v_mov_b32_e32 v56, v97
	v_mov_b32_e32 v55, v97
	v_mov_b32_e32 v54, v97
	s_waitcnt lgkmcnt(0)
	v_mov_b32_e32 v53, v97
	v_mov_b32_e32 v52, v97
	v_mov_b32_e32 v51, v97
	v_mov_b32_e32 v50, v97
	s_cbranch_vccnz .LBB4_23
	v_mov_b32_e32 v50, 0
	v_lshl_add_u64 v[98:99], s[26:27], 0, v[0:1]
	v_lshl_add_u64 v[100:101], s[26:27], 0, v[120:121]
	v_lshl_add_u64 v[102:103], s[28:29], 0, v[122:123]
	v_lshl_add_u64 v[104:105], s[28:29], 0, v[124:125]
	v_lshl_add_u64 v[106:107], s[28:29], 0, v[126:127]
	s_mov_b32 s67, 0
	s_mov_b64 s[30:31], 0
	v_mov_b32_e32 v51, v50
	v_mov_b32_e32 v52, v50
	v_mov_b32_e32 v53, v50
	v_mov_b32_e32 v54, v50
	v_mov_b32_e32 v55, v50
	v_mov_b32_e32 v56, v50
	v_mov_b32_e32 v57, v50
	v_mov_b32_e32 v58, v50
	v_mov_b32_e32 v59, v50
	v_mov_b32_e32 v60, v50
	v_mov_b32_e32 v61, v50
	v_mov_b32_e32 v62, v50
	v_mov_b32_e32 v63, v50
	v_mov_b32_e32 v64, v50
	v_mov_b32_e32 v65, v50
	v_mov_b32_e32 v66, v50
	v_mov_b32_e32 v67, v50
	v_mov_b32_e32 v68, v50
	v_mov_b32_e32 v69, v50
	v_mov_b32_e32 v70, v50
	v_mov_b32_e32 v71, v50
	v_mov_b32_e32 v72, v50
	v_mov_b32_e32 v73, v50
	v_mov_b32_e32 v74, v50
	v_mov_b32_e32 v75, v50
	v_mov_b32_e32 v76, v50
	v_mov_b32_e32 v77, v50
	v_mov_b32_e32 v78, v50
	v_mov_b32_e32 v79, v50
	v_mov_b32_e32 v80, v50
	v_mov_b32_e32 v81, v50
	v_mov_b32_e32 v82, v50
	v_mov_b32_e32 v83, v50
	v_mov_b32_e32 v84, v50
	v_mov_b32_e32 v85, v50
	v_mov_b32_e32 v86, v50
	v_mov_b32_e32 v87, v50
	v_mov_b32_e32 v88, v50
	v_mov_b32_e32 v89, v50
	v_mov_b32_e32 v90, v50
	v_mov_b32_e32 v91, v50
	v_mov_b32_e32 v92, v50
	v_mov_b32_e32 v93, v50
	v_mov_b32_e32 v94, v50
	v_mov_b32_e32 v95, v50
	v_mov_b32_e32 v96, v50
	v_mov_b32_e32 v97, v50
	s_add_u32 s34, s26, s30
	s_addc_u32 s35, s27, s31
	s_add_u32 s34, s34, 0x180
	s_addc_u32 s35, s35, 0
	s_add_u32 s68, s28, s30
	s_addc_u32 s69, s29, s31
	s_add_u32 s70, s68, 0x180
	s_addc_u32 s71, s69, 0
	s_cmp_eq_u32 s60, s67
	s_cselect_b32 s69, s5, s35
	s_cselect_b32 s68, s4, s34
	s_cselect_b32 s35, s7, s71
	s_cselect_b32 s34, s6, s70
	s_add_i32 s70, s62, s44
	v_lshl_add_u64 v[108:109], v[98:99], 0, s[30:31]
.LBB4_22:
	s_mov_b32 m0, s70
	ds_read_b128 v[130:133], v136 offset:16384
	ds_read_b128 v[142:145], v136 offset:17408
	ds_read_b128 v[146:149], v136 offset:18432
	ds_read_b128 v[150:153], v136 offset:19456
	ds_read_b128 v[154:157], v137
	ds_read_b128 v[158:161], v137 offset:1024
	ds_read_b128 v[162:165], v137 offset:2048
	ds_read_b128 v[166:169], v137 offset:3072
	ds_read_b128 v[170:173], v137 offset:4096
	ds_read_b128 v[174:177], v137 offset:5120
	ds_read_b128 v[178:181], v137 offset:6144
	ds_read_b128 v[182:185], v137 offset:7168
	global_load_lds_dwordx4 v[108:109], off
	v_lshl_add_u64 v[108:109], v[100:101], 0, s[30:31]
	s_add_i32 m0, s70, 0x2000
	s_nop 0
	global_load_lds_dwordx4 v[108:109], off
	s_barrier
	s_waitcnt lgkmcnt(0)
	s_setprio 1
	s_waitcnt lgkmcnt(0)
	v_mfma_f32_16x16x32_f16 v[94:97], v[130:133], v[154:157], v[94:97]
	v_mfma_f32_16x16x32_f16 v[90:93], v[146:149], v[154:157], v[90:93]
	v_mfma_f32_16x16x32_f16 v[82:85], v[130:133], v[162:165], v[82:85]
	v_mfma_f32_16x16x32_f16 v[78:81], v[146:149], v[162:165], v[78:81]
	v_mfma_f32_16x16x32_f16 v[70:73], v[130:133], v[170:173], v[70:73]
	v_mfma_f32_16x16x32_f16 v[66:69], v[146:149], v[170:173], v[66:69]
	v_mfma_f32_16x16x32_f16 v[58:61], v[130:133], v[178:181], v[58:61]
	v_mfma_f32_16x16x32_f16 v[54:57], v[146:149], v[178:181], v[54:57]
	v_mfma_f32_16x16x32_f16 v[94:97], v[142:145], v[158:161], v[94:97]
	v_mfma_f32_16x16x32_f16 v[90:93], v[150:153], v[158:161], v[90:93]
	v_mfma_f32_16x16x32_f16 v[82:85], v[142:145], v[166:169], v[82:85]
	v_mfma_f32_16x16x32_f16 v[78:81], v[150:153], v[166:169], v[78:81]
	v_mfma_f32_16x16x32_f16 v[70:73], v[142:145], v[174:177], v[70:73]
	v_mfma_f32_16x16x32_f16 v[66:69], v[150:153], v[174:177], v[66:69]
	v_mfma_f32_16x16x32_f16 v[58:61], v[142:145], v[182:185], v[58:61]
	v_mfma_f32_16x16x32_f16 v[54:57], v[150:153], v[182:185], v[54:57]
	s_setprio 0
	s_barrier
	v_lshl_add_u64 v[108:109], v[102:103], 0, s[30:31]
	s_add_i32 m0, s49, 0x18000
	ds_read_b128 v[130:133], v136 offset:20480
	ds_read_b128 v[142:145], v136 offset:21504
	global_load_lds_dwordx4 v[108:109], off
	v_lshl_add_u64 v[108:109], v[104:105], 0, s[30:31]
	s_add_i32 m0, s49, 0x1a000
	s_nop 0
	global_load_lds_dwordx4 v[108:109], off
	v_lshl_add_u64 v[108:109], v[106:107], 0, s[30:31]
	s_add_i32 m0, s49, 0x1c000
	s_nop 0
	global_load_lds_dwordx4 v[108:109], off
	s_cmp_lg_u32 s67, 0
	s_cbranch_scc1 .Lpj_norm_0
	s_mul_i32 s72, s66, 0xc0
	v_add_u32_e32 v214, s72, v135
	v_ashrrev_i32_e32 v215, 31, v214
	v_lshl_add_u64 v[214:215], v[214:215], 2, s[10:11]
	global_load_dwordx4 v[202:205], v[214:215], off
	global_load_dwordx4 v[206:209], v[214:215], off offset:64
	global_load_dwordx4 v[210:213], v[214:215], off offset:128
	global_load_dwordx4 v[2:5], v[194:195], off
	global_load_dwordx4 v[6:9], v[194:195], off offset:64
	global_load_dwordx4 v[10:13], v[194:195], off offset:128
	global_load_dwordx4 v[14:17], v[196:197], off
	s_waitcnt vmcnt(12)
	s_branch .Lpj_join_0

.Lpj_join_2:
	s_barrier
	s_waitcnt lgkmcnt(0)
	s_setprio 1
	s_waitcnt lgkmcnt(0)
	v_mfma_f32_16x16x32_f16 v[86:89], v[130:133], v[154:157], v[86:89]
	v_mfma_f32_16x16x32_f16 v[74:77], v[130:133], v[162:165], v[74:77]
	v_mfma_f32_16x16x32_f16 v[62:65], v[130:133], v[170:173], v[62:65]
	v_mfma_f32_16x16x32_f16 v[50:53], v[130:133], v[178:181], v[50:53]
	v_mfma_f32_16x16x32_f16 v[86:89], v[142:145], v[158:161], v[86:89]
	v_mfma_f32_16x16x32_f16 v[74:77], v[142:145], v[166:169], v[74:77]
	v_mfma_f32_16x16x32_f16 v[62:65], v[142:145], v[174:177], v[62:65]
	v_mfma_f32_16x16x32_f16 v[50:53], v[142:145], v[182:185], v[50:53]
	s_setprio 0
	s_add_i32 s67, s67, 3
	s_add_u32 s30, s30, 0x180
	s_addc_u32 s31, s31, 0
	s_cmp_ge_i32 s67, s59
	s_cbranch_scc1 .Lrot_exit_proj
	s_add_u32 s34, s26, s30
	s_addc_u32 s35, s27, s31
	s_add_u32 s34, s34, 0x180
	s_addc_u32 s35, s35, 0
	s_add_u32 s68, s28, s30
	s_addc_u32 s69, s29, s31
	s_add_u32 s70, s68, 0x180
	s_addc_u32 s71, s69, 0
	s_cmp_eq_u32 s60, s67
	s_cselect_b32 s69, s5, s35
	s_cselect_b32 s68, s4, s34
	s_cselect_b32 s35, s7, s71
	s_cselect_b32 s34, s6, s70
	s_add_i32 s70, s62, s44
	v_lshl_add_u64 v[108:109], v[98:99], 0, s[30:31]
	s_barrier
	s_branch .LBB4_22

.LBB5_53:
	v_mov_b32_e32 v95, 0
	s_andn2_b64 vcc, exec, s[24:25]
	v_mov_b32_e32 v94, v95
	v_mov_b32_e32 v93, v95
	v_mov_b32_e32 v92, v95
	v_mov_b32_e32 v91, v95
	v_mov_b32_e32 v90, v95
	v_mov_b32_e32 v89, v95
	v_mov_b32_e32 v88, v95
	v_mov_b32_e32 v79, v95
	v_mov_b32_e32 v78, v95
	v_mov_b32_e32 v77, v95
	v_mov_b32_e32 v76, v95
	v_mov_b32_e32 v75, v95
	v_mov_b32_e32 v74, v95
	v_mov_b32_e32 v73, v95
	v_mov_b32_e32 v72, v95
	v_mov_b32_e32 v31, v95
	v_mov_b32_e32 v30, v95
	v_mov_b32_e32 v29, v95
	v_mov_b32_e32 v28, v95
	v_mov_b32_e32 v27, v95
	v_mov_b32_e32 v26, v95
	v_mov_b32_e32 v25, v95
	v_mov_b32_e32 v24, v95
	v_mov_b32_e32 v15, v95
	v_mov_b32_e32 v14, v95
	v_mov_b32_e32 v13, v95
	v_mov_b32_e32 v12, v95
	v_mov_b32_e32 v11, v95
	v_mov_b32_e32 v10, v95
	v_mov_b32_e32 v9, v95
	v_mov_b32_e32 v8, v95
	v_mov_b32_e32 v87, v95
	v_mov_b32_e32 v86, v95
	v_mov_b32_e32 v85, v95
	v_mov_b32_e32 v84, v95
	v_mov_b32_e32 v83, v95
	v_mov_b32_e32 v82, v95
	v_mov_b32_e32 v81, v95
	v_mov_b32_e32 v80, v95
	v_mov_b32_e32 v55, v95
	v_mov_b32_e32 v54, v95
	v_mov_b32_e32 v53, v95
	v_mov_b32_e32 v52, v95
	v_mov_b32_e32 v51, v95
	v_mov_b32_e32 v50, v95
	v_mov_b32_e32 v49, v95
	v_mov_b32_e32 v48, v95
	v_mov_b32_e32 v23, v95
	v_mov_b32_e32 v22, v95
	v_mov_b32_e32 v21, v95
	v_mov_b32_e32 v20, v95
	v_mov_b32_e32 v19, v95
	v_mov_b32_e32 v18, v95
	v_mov_b32_e32 v17, v95
	v_mov_b32_e32 v16, v95
	v_mov_b32_e32 v7, v95
	v_mov_b32_e32 v6, v95
	v_mov_b32_e32 v5, v95
	v_mov_b32_e32 v4, v95
	v_mov_b32_e32 v3, v95
	v_mov_b32_e32 v2, v95
	v_mov_b32_e32 v1, v95
	v_mov_b32_e32 v0, v95
	s_cbranch_vccnz .LBB5_42
	v_mov_b32_e32 v0, 0
	v_lshl_add_u64 v[32:33], s[40:41], 0, v[112:113]
	v_lshl_add_u64 v[34:35], s[40:41], 0, v[114:115]
	v_lshl_add_u64 v[36:37], s[42:43], 0, v[116:117]
	v_lshl_add_u64 v[38:39], s[42:43], 0, v[118:119]
	v_lshl_add_u64 v[40:41], s[42:43], 0, v[120:121]
	v_lshl_add_u64 v[42:43], s[42:43], 0, v[122:123]
	s_mov_b32 s75, 0
	s_mov_b64 s[44:45], 0
	v_mov_b32_e32 v1, v0
	v_mov_b32_e32 v2, v0
	v_mov_b32_e32 v3, v0
	v_mov_b32_e32 v4, v0
	v_mov_b32_e32 v5, v0
	v_mov_b32_e32 v6, v0
	v_mov_b32_e32 v7, v0
	v_mov_b32_e32 v16, v0
	v_mov_b32_e32 v17, v0
	v_mov_b32_e32 v18, v0
	v_mov_b32_e32 v19, v0
	v_mov_b32_e32 v20, v0
	v_mov_b32_e32 v21, v0
	v_mov_b32_e32 v22, v0
	v_mov_b32_e32 v23, v0
	v_mov_b32_e32 v48, v0
	v_mov_b32_e32 v49, v0
	v_mov_b32_e32 v50, v0
	v_mov_b32_e32 v51, v0
	v_mov_b32_e32 v52, v0
	v_mov_b32_e32 v53, v0
	v_mov_b32_e32 v54, v0
	v_mov_b32_e32 v55, v0
	v_mov_b32_e32 v80, v0
	v_mov_b32_e32 v81, v0
	v_mov_b32_e32 v82, v0
	v_mov_b32_e32 v83, v0
	v_mov_b32_e32 v84, v0
	v_mov_b32_e32 v85, v0
	v_mov_b32_e32 v86, v0
	v_mov_b32_e32 v87, v0
	v_mov_b32_e32 v8, v0
	v_mov_b32_e32 v9, v0
	v_mov_b32_e32 v10, v0
	v_mov_b32_e32 v11, v0
	v_mov_b32_e32 v12, v0
	v_mov_b32_e32 v13, v0
	v_mov_b32_e32 v14, v0
	v_mov_b32_e32 v15, v0
	v_mov_b32_e32 v24, v0
	v_mov_b32_e32 v25, v0
	v_mov_b32_e32 v26, v0
	v_mov_b32_e32 v27, v0
	v_mov_b32_e32 v28, v0
	v_mov_b32_e32 v29, v0
	v_mov_b32_e32 v30, v0
	v_mov_b32_e32 v31, v0
	v_mov_b32_e32 v72, v0
	v_mov_b32_e32 v73, v0
	v_mov_b32_e32 v74, v0
	v_mov_b32_e32 v75, v0
	v_mov_b32_e32 v76, v0
	v_mov_b32_e32 v77, v0
	v_mov_b32_e32 v78, v0
	v_mov_b32_e32 v79, v0
	v_mov_b32_e32 v88, v0
	v_mov_b32_e32 v89, v0
	v_mov_b32_e32 v90, v0
	v_mov_b32_e32 v91, v0
	v_mov_b32_e32 v92, v0
	v_mov_b32_e32 v93, v0
	v_mov_b32_e32 v94, v0
	v_mov_b32_e32 v95, v0
	s_add_u32 s46, s40, s44
	s_addc_u32 s47, s41, s45
	s_add_u32 s46, s46, 0x180
	s_addc_u32 s47, s47, 0
	s_add_u32 s48, s42, s44
	s_addc_u32 s49, s43, s45
	s_add_u32 s76, s48, 0x180
	s_addc_u32 s77, s49, 0
	s_cmp_eq_u32 s67, s75
	s_cselect_b32 s49, s7, s47
	s_cselect_b32 s48, s6, s46
	s_cselect_b32 s47, s5, s77
	s_cselect_b32 s46, s4, s76
	s_add_i32 s76, s19, s54
	v_lshl_add_u64 v[126:127], v[32:33], 0, s[44:45]
.LBB5_55:
	s_mov_b32 m0, s76
	ds_read_b128 v[44:47], v130 offset:16384
	ds_read_b128 v[56:59], v130 offset:17408
	ds_read_b128 v[60:63], v130 offset:18432
	ds_read_b128 v[64:67], v130 offset:19456
	ds_read_b128 v[68:71], v131
	ds_read_b128 v[96:99], v131 offset:1024
	ds_read_b128 v[136:139], v131 offset:2048
	ds_read_b128 v[140:143], v131 offset:3072
	ds_read_b128 v[144:147], v131 offset:4096
	ds_read_b128 v[148:151], v131 offset:5120
	ds_read_b128 v[152:155], v131 offset:6144
	ds_read_b128 v[156:159], v131 offset:7168
	global_load_lds_dwordx4 v[126:127], off
	v_lshl_add_u64 v[126:127], v[34:35], 0, s[44:45]
	s_add_i32 m0, s76, 0x2000
	s_add_i32 s76, s27, s54
	global_load_lds_dwordx4 v[126:127], off
	v_lshl_add_u64 v[126:127], v[36:37], 0, s[44:45]
	s_mov_b32 m0, s76
	s_nop 0
	global_load_lds_dwordx4 v[126:127], off
	v_lshl_add_u64 v[126:127], v[38:39], 0, s[44:45]
	s_add_i32 m0, s76, 0x2000
	s_nop 0
	global_load_lds_dwordx4 v[126:127], off
	s_barrier
	s_waitcnt lgkmcnt(0)
	s_setprio 1
	s_waitcnt lgkmcnt(0)
	v_mfma_f32_16x16x32_f16 v[92:95], v[44:47], v[68:71], v[92:95]
	v_mfma_f32_16x16x32_f16 v[88:91], v[60:63], v[68:71], v[88:91]
	v_mfma_f32_16x16x32_f16 v[76:79], v[44:47], v[136:139], v[76:79]
	v_mfma_f32_16x16x32_f16 v[72:75], v[60:63], v[136:139], v[72:75]
	v_mfma_f32_16x16x32_f16 v[28:31], v[44:47], v[144:147], v[28:31]
	v_mfma_f32_16x16x32_f16 v[24:27], v[60:63], v[144:147], v[24:27]
	v_mfma_f32_16x16x32_f16 v[12:15], v[44:47], v[152:155], v[12:15]
	v_mfma_f32_16x16x32_f16 v[8:11], v[60:63], v[152:155], v[8:11]
	v_mfma_f32_16x16x32_f16 v[92:95], v[56:59], v[96:99], v[92:95]
	v_mfma_f32_16x16x32_f16 v[88:91], v[64:67], v[96:99], v[88:91]
	v_mfma_f32_16x16x32_f16 v[76:79], v[56:59], v[140:143], v[76:79]
	v_mfma_f32_16x16x32_f16 v[72:75], v[64:67], v[140:143], v[72:75]
	v_mfma_f32_16x16x32_f16 v[28:31], v[56:59], v[148:151], v[28:31]
	v_mfma_f32_16x16x32_f16 v[24:27], v[64:67], v[148:151], v[24:27]
	v_mfma_f32_16x16x32_f16 v[12:15], v[56:59], v[156:159], v[12:15]
	v_mfma_f32_16x16x32_f16 v[8:11], v[64:67], v[156:159], v[8:11]
	s_setprio 0
	s_barrier
	s_add_i32 s76, s68, s54
	v_lshl_add_u64 v[126:127], v[40:41], 0, s[44:45]
	s_mov_b32 m0, s76
	ds_read_b128 v[44:47], v130 offset:32768
	ds_read_b128 v[56:59], v130 offset:33792
	ds_read_b128 v[60:63], v130 offset:34816
	ds_read_b128 v[64:67], v130 offset:35840
	global_load_lds_dwordx4 v[126:127], off
	v_lshl_add_u64 v[126:127], v[42:43], 0, s[44:45]
	s_add_i32 m0, s76, 0x2000
	s_nop 0
	global_load_lds_dwordx4 v[126:127], off
	s_waitcnt vmcnt(6)
	s_barrier
	s_waitcnt lgkmcnt(0)
	s_setprio 1
	s_waitcnt lgkmcnt(0)
	v_mfma_f32_16x16x32_f16 v[84:87], v[44:47], v[68:71], v[84:87]
	v_mfma_f32_16x16x32_f16 v[52:55], v[44:47], v[136:139], v[52:55]
	v_mfma_f32_16x16x32_f16 v[48:51], v[60:63], v[136:139], v[48:51]
	v_mfma_f32_16x16x32_f16 v[20:23], v[44:47], v[144:147], v[20:23]
	v_mfma_f32_16x16x32_f16 v[16:19], v[60:63], v[144:147], v[16:19]
	v_mfma_f32_16x16x32_f16 v[4:7], v[44:47], v[152:155], v[4:7]
	v_mfma_f32_16x16x32_f16 v[0:3], v[60:63], v[152:155], v[0:3]
	v_mfma_f32_16x16x32_f16 v[84:87], v[56:59], v[96:99], v[84:87]
	v_mfma_f32_16x16x32_f16 v[68:71], v[60:63], v[68:71], v[80:83]
	v_mfma_f32_16x16x32_f16 v[52:55], v[56:59], v[140:143], v[52:55]
	v_mfma_f32_16x16x32_f16 v[48:51], v[64:67], v[140:143], v[48:51]
	v_mfma_f32_16x16x32_f16 v[20:23], v[56:59], v[148:151], v[20:23]
	v_mfma_f32_16x16x32_f16 v[16:19], v[64:67], v[148:151], v[16:19]
	v_mfma_f32_16x16x32_f16 v[4:7], v[56:59], v[156:159], v[4:7]
	v_mfma_f32_16x16x32_f16 v[0:3], v[64:67], v[156:159], v[0:3]
	v_mfma_f32_16x16x32_f16 v[68:71], v[64:67], v[96:99], v[68:71]
	s_setprio 0
	s_barrier
	s_add_i32 s76, 0, 0x10000
	s_mov_b32 m0, s57
	v_add_u32_e32 v64, s76, v128
	v_lshl_add_u64 v[126:127], s[48:49], 0, v[100:101]
	ds_read_b128 v[44:47], v64
	ds_read_b128 v[56:59], v64 offset:1024
	ds_read_b128 v[60:63], v64 offset:2048
	ds_read_b128 v[64:67], v64 offset:3072
	ds_read_b128 v[80:83], v131 offset:49152
	ds_read_b128 v[96:99], v131 offset:50176
	ds_read_b128 v[136:139], v131 offset:51200
	ds_read_b128 v[140:143], v131 offset:52224
	ds_read_b128 v[144:147], v131 offset:53248
	ds_read_b128 v[148:151], v131 offset:54272
	ds_read_b128 v[152:155], v131 offset:55296
	ds_read_b128 v[156:159], v131 offset:56320
	global_load_lds_dwordx4 v[126:127], off
	v_lshl_add_u64 v[160:161], s[48:49], 0, v[104:105]
	s_mov_b32 m0, s58
	v_lshl_add_u64 v[162:163], s[46:47], 0, v[102:103]
	global_load_lds_dwordx4 v[160:161], off
	s_mov_b32 m0, s59
	v_lshl_add_u64 v[164:165], s[46:47], 0, v[106:107]
	global_load_lds_dwordx4 v[162:163], off
	s_mov_b32 m0, s60
	s_nop 0
	global_load_lds_dwordx4 v[164:165], off
	s_barrier
	s_waitcnt lgkmcnt(0)
	s_setprio 1
	s_waitcnt lgkmcnt(0)
	v_mfma_f32_16x16x32_f16 v[92:95], v[44:47], v[80:83], v[92:95]
	v_mfma_f32_16x16x32_f16 v[88:91], v[60:63], v[80:83], v[88:91]
	v_mfma_f32_16x16x32_f16 v[76:79], v[44:47], v[136:139], v[76:79]
	v_mfma_f32_16x16x32_f16 v[72:75], v[60:63], v[136:139], v[72:75]
	v_mfma_f32_16x16x32_f16 v[28:31], v[44:47], v[144:147], v[28:31]
	v_mfma_f32_16x16x32_f16 v[24:27], v[60:63], v[144:147], v[24:27]
	v_mfma_f32_16x16x32_f16 v[12:15], v[44:47], v[152:155], v[12:15]
	v_mfma_f32_16x16x32_f16 v[8:11], v[60:63], v[152:155], v[8:11]
	v_mfma_f32_16x16x32_f16 v[92:95], v[56:59], v[96:99], v[92:95]
	v_mfma_f32_16x16x32_f16 v[88:91], v[64:67], v[96:99], v[88:91]
	v_mfma_f32_16x16x32_f16 v[76:79], v[56:59], v[140:143], v[76:79]
	v_mfma_f32_16x16x32_f16 v[72:75], v[64:67], v[140:143], v[72:75]
	v_mfma_f32_16x16x32_f16 v[28:31], v[56:59], v[148:151], v[28:31]
	v_mfma_f32_16x16x32_f16 v[24:27], v[64:67], v[148:151], v[24:27]
	v_mfma_f32_16x16x32_f16 v[12:15], v[56:59], v[156:159], v[12:15]
	v_mfma_f32_16x16x32_f16 v[8:11], v[64:67], v[156:159], v[8:11]
	s_setprio 0
	s_barrier
	s_add_i32 s48, 0, 0x14000
	s_add_u32 s46, s46, s10
	s_addc_u32 s47, s47, s11
	s_mov_b32 m0, s61
	v_add_u32_e32 v64, s48, v128
	v_lshl_add_u64 v[166:167], s[46:47], 0, v[102:103]
	ds_read_b128 v[44:47], v64
	ds_read_b128 v[56:59], v64 offset:1024
	ds_read_b128 v[60:63], v64 offset:2048
	ds_read_b128 v[64:67], v64 offset:3072
	global_load_lds_dwordx4 v[166:167], off
	v_lshl_add_u64 v[168:169], s[46:47], 0, v[106:107]
	s_mov_b32 m0, s62
	s_nop 0
	global_load_lds_dwordx4 v[168:169], off
	s_waitcnt vmcnt(6)
	s_barrier
	s_waitcnt lgkmcnt(0)
	s_setprio 1
	s_waitcnt lgkmcnt(0)
	v_mfma_f32_16x16x32_f16 v[84:87], v[44:47], v[80:83], v[84:87]
	v_mfma_f32_16x16x32_f16 v[52:55], v[44:47], v[136:139], v[52:55]
	v_mfma_f32_16x16x32_f16 v[48:51], v[60:63], v[136:139], v[48:51]
	v_mfma_f32_16x16x32_f16 v[20:23], v[44:47], v[144:147], v[20:23]
	v_mfma_f32_16x16x32_f16 v[16:19], v[60:63], v[144:147], v[16:19]
	v_mfma_f32_16x16x32_f16 v[4:7], v[44:47], v[152:155], v[4:7]
	v_mfma_f32_16x16x32_f16 v[0:3], v[60:63], v[152:155], v[0:3]
	v_mfma_f32_16x16x32_f16 v[84:87], v[56:59], v[96:99], v[84:87]
	v_mfma_f32_16x16x32_f16 v[68:71], v[60:63], v[80:83], v[68:71]
	v_mfma_f32_16x16x32_f16 v[52:55], v[56:59], v[140:143], v[52:55]
	v_mfma_f32_16x16x32_f16 v[48:51], v[64:67], v[140:143], v[48:51]
	v_mfma_f32_16x16x32_f16 v[20:23], v[56:59], v[148:151], v[20:23]
	v_mfma_f32_16x16x32_f16 v[16:19], v[64:67], v[148:151], v[16:19]
	v_mfma_f32_16x16x32_f16 v[4:7], v[56:59], v[156:159], v[4:7]
	v_mfma_f32_16x16x32_f16 v[0:3], v[64:67], v[156:159], v[0:3]
	v_mfma_f32_16x16x32_f16 v[68:71], v[64:67], v[96:99], v[68:71]
	s_setprio 0
	s_barrier
	s_mov_b32 m0, s64
	v_lshl_add_u64 v[126:127], v[126:127], 0, s[22:23]
	ds_read_b128 v[44:47], v132
	ds_read_b128 v[56:59], v132 offset:1024
	ds_read_b128 v[60:63], v132 offset:2048
	ds_read_b128 v[64:67], v132 offset:3072
	ds_read_b128 v[80:83], v133
	ds_read_b128 v[96:99], v133 offset:1024
	ds_read_b128 v[136:139], v133 offset:2048
	ds_read_b128 v[140:143], v133 offset:3072
	ds_read_b128 v[144:147], v133 offset:4096
	ds_read_b128 v[148:151], v133 offset:5120
	ds_read_b128 v[152:155], v133 offset:6144
	ds_read_b128 v[156:159], v133 offset:7168
	global_load_lds_dwordx4 v[126:127], off
	v_lshl_add_u64 v[126:127], v[160:161], 0, s[22:23]
	s_mov_b32 m0, s65
	s_add_i32 s46, s76, s54
	global_load_lds_dwordx4 v[126:127], off
	v_lshl_add_u64 v[126:127], v[162:163], 0, s[22:23]
	s_mov_b32 m0, s46
	s_nop 0
	global_load_lds_dwordx4 v[126:127], off
	v_lshl_add_u64 v[126:127], v[164:165], 0, s[22:23]
	s_add_i32 m0, s46, 0x2000
	s_nop 0
	global_load_lds_dwordx4 v[126:127], off
	s_barrier
	s_waitcnt lgkmcnt(0)
	s_setprio 1
	s_waitcnt lgkmcnt(0)
	v_mfma_f32_16x16x32_f16 v[92:95], v[44:47], v[80:83], v[92:95]
	v_mfma_f32_16x16x32_f16 v[88:91], v[60:63], v[80:83], v[88:91]
	v_mfma_f32_16x16x32_f16 v[76:79], v[44:47], v[136:139], v[76:79]
	v_mfma_f32_16x16x32_f16 v[72:75], v[60:63], v[136:139], v[72:75]
	v_mfma_f32_16x16x32_f16 v[28:31], v[44:47], v[144:147], v[28:31]
	v_mfma_f32_16x16x32_f16 v[24:27], v[60:63], v[144:147], v[24:27]
	v_mfma_f32_16x16x32_f16 v[12:15], v[44:47], v[152:155], v[12:15]
	v_mfma_f32_16x16x32_f16 v[8:11], v[60:63], v[152:155], v[8:11]
	v_mfma_f32_16x16x32_f16 v[92:95], v[56:59], v[96:99], v[92:95]
	v_mfma_f32_16x16x32_f16 v[88:91], v[64:67], v[96:99], v[88:91]
	v_mfma_f32_16x16x32_f16 v[76:79], v[56:59], v[140:143], v[76:79]
	v_mfma_f32_16x16x32_f16 v[72:75], v[64:67], v[140:143], v[72:75]
	v_mfma_f32_16x16x32_f16 v[28:31], v[56:59], v[148:151], v[28:31]
	v_mfma_f32_16x16x32_f16 v[24:27], v[64:67], v[148:151], v[24:27]
	v_mfma_f32_16x16x32_f16 v[12:15], v[56:59], v[156:159], v[12:15]
	v_mfma_f32_16x16x32_f16 v[8:11], v[64:67], v[156:159], v[8:11]
	s_setprio 0
	s_barrier
	s_add_i32 s46, s48, s54
	v_lshl_add_u64 v[126:127], v[166:167], 0, s[22:23]
	s_mov_b32 m0, s46
	ds_read_b128 v[44:47], v134
	ds_read_b128 v[56:59], v134 offset:1024
	ds_read_b128 v[60:63], v134 offset:2048
	ds_read_b128 v[64:67], v134 offset:3072
	global_load_lds_dwordx4 v[126:127], off
	v_lshl_add_u64 v[126:127], v[168:169], 0, s[22:23]
	s_add_i32 m0, s46, 0x2000
	s_nop 0
	global_load_lds_dwordx4 v[126:127], off
	s_waitcnt vmcnt(6)
	s_barrier
	s_waitcnt lgkmcnt(0)
	s_setprio 1
	s_waitcnt lgkmcnt(0)
	v_mfma_f32_16x16x32_f16 v[84:87], v[44:47], v[80:83], v[84:87]
	v_mfma_f32_16x16x32_f16 v[68:71], v[60:63], v[80:83], v[68:71]
	v_mfma_f32_16x16x32_f16 v[52:55], v[44:47], v[136:139], v[52:55]
	v_mfma_f32_16x16x32_f16 v[48:51], v[60:63], v[136:139], v[48:51]
	v_mfma_f32_16x16x32_f16 v[20:23], v[44:47], v[144:147], v[20:23]
	v_mfma_f32_16x16x32_f16 v[16:19], v[60:63], v[144:147], v[16:19]
	v_mfma_f32_16x16x32_f16 v[4:7], v[44:47], v[152:155], v[4:7]
	v_mfma_f32_16x16x32_f16 v[0:3], v[60:63], v[152:155], v[0:3]
	v_mfma_f32_16x16x32_f16 v[84:87], v[56:59], v[96:99], v[84:87]
	v_mfma_f32_16x16x32_f16 v[80:83], v[64:67], v[96:99], v[68:71]
	v_mfma_f32_16x16x32_f16 v[52:55], v[56:59], v[140:143], v[52:55]
	v_mfma_f32_16x16x32_f16 v[48:51], v[64:67], v[140:143], v[48:51]
	v_mfma_f32_16x16x32_f16 v[20:23], v[56:59], v[148:151], v[20:23]
	v_mfma_f32_16x16x32_f16 v[16:19], v[64:67], v[148:151], v[16:19]
	v_mfma_f32_16x16x32_f16 v[4:7], v[56:59], v[156:159], v[4:7]
	v_mfma_f32_16x16x32_f16 v[0:3], v[64:67], v[156:159], v[0:3]
	s_setprio 0
	s_add_i32 s75, s75, 3
	s_add_u32 s44, s44, 0x180
	s_addc_u32 s45, s45, 0
	s_cmp_ge_i32 s75, s66
	s_cbranch_scc1 .Lrot_exit_mlp1
	s_add_u32 s46, s40, s44
	s_addc_u32 s47, s41, s45
	s_add_u32 s46, s46, 0x180
	s_addc_u32 s47, s47, 0
	s_add_u32 s48, s42, s44
	s_addc_u32 s49, s43, s45
	s_add_u32 s76, s48, 0x180
	s_addc_u32 s77, s49, 0
	s_cmp_eq_u32 s67, s75
	s_cselect_b32 s49, s7, s47
	s_cselect_b32 s48, s6, s46
	s_cselect_b32 s47, s5, s77
	s_cselect_b32 s46, s4, s76
	s_add_i32 s76, s19, s54
	v_lshl_add_u64 v[126:127], v[32:33], 0, s[44:45]
	s_barrier
	s_branch .LBB5_55

.LBB6_20:
	v_mov_b32_e32 v43, 0
	s_andn2_b64 vcc, exec, s[6:7]
	v_mov_b32_e32 v42, v43
	v_mov_b32_e32 v41, v43
	v_mov_b32_e32 v40, v43
	v_mov_b32_e32 v47, v43
	v_mov_b32_e32 v46, v43
	v_mov_b32_e32 v45, v43
	v_mov_b32_e32 v44, v43
	v_mov_b32_e32 v39, v43
	v_mov_b32_e32 v38, v43
	v_mov_b32_e32 v37, v43
	v_mov_b32_e32 v36, v43
	v_mov_b32_e32 v35, v43
	v_mov_b32_e32 v34, v43
	v_mov_b32_e32 v33, v43
	v_mov_b32_e32 v32, v43
	v_mov_b32_e32 v31, v43
	v_mov_b32_e32 v30, v43
	v_mov_b32_e32 v29, v43
	v_mov_b32_e32 v28, v43
	v_mov_b32_e32 v27, v43
	v_mov_b32_e32 v26, v43
	v_mov_b32_e32 v25, v43
	v_mov_b32_e32 v24, v43
	v_mov_b32_e32 v23, v43
	v_mov_b32_e32 v22, v43
	v_mov_b32_e32 v21, v43
	v_mov_b32_e32 v20, v43
	v_mov_b32_e32 v19, v43
	v_mov_b32_e32 v18, v43
	v_mov_b32_e32 v17, v43
	v_mov_b32_e32 v16, v43
	v_mov_b32_e32 v15, v43
	v_mov_b32_e32 v14, v43
	v_mov_b32_e32 v13, v43
	v_mov_b32_e32 v12, v43
	v_mov_b32_e32 v11, v43
	v_mov_b32_e32 v10, v43
	v_mov_b32_e32 v9, v43
	v_mov_b32_e32 v8, v43
	v_mov_b32_e32 v7, v43
	v_mov_b32_e32 v6, v43
	v_mov_b32_e32 v5, v43
	v_mov_b32_e32 v4, v43
	v_mov_b32_e32 v3, v43
	v_mov_b32_e32 v2, v43
	v_mov_b32_e32 v1, v43
	v_mov_b32_e32 v0, v43
	s_cbranch_vccnz .LBB6_9
	v_mov_b32_e32 v0, 0
	v_lshl_add_u64 v[116:117], s[22:23], 0, v[106:107]
	v_lshl_add_u64 v[118:119], s[22:23], 0, v[108:109]
	v_lshl_add_u64 v[120:121], s[24:25], 0, v[110:111]
	v_lshl_add_u64 v[122:123], s[24:25], 0, v[112:113]
	v_lshl_add_u64 v[124:125], s[24:25], 0, v[114:115]
	s_mov_b32 s65, 0
	s_mov_b64 s[28:29], 0
	v_mov_b32_e32 v1, v0
	v_mov_b32_e32 v2, v0
	v_mov_b32_e32 v3, v0
	v_mov_b32_e32 v4, v0
	v_mov_b32_e32 v5, v0
	v_mov_b32_e32 v6, v0
	v_mov_b32_e32 v7, v0
	v_mov_b32_e32 v8, v0
	v_mov_b32_e32 v9, v0
	v_mov_b32_e32 v10, v0
	v_mov_b32_e32 v11, v0
	v_mov_b32_e32 v12, v0
	v_mov_b32_e32 v13, v0
	v_mov_b32_e32 v14, v0
	v_mov_b32_e32 v15, v0
	v_mov_b32_e32 v16, v0
	v_mov_b32_e32 v17, v0
	v_mov_b32_e32 v18, v0
	v_mov_b32_e32 v19, v0
	v_mov_b32_e32 v20, v0
	v_mov_b32_e32 v21, v0
	v_mov_b32_e32 v22, v0
	v_mov_b32_e32 v23, v0
	v_mov_b32_e32 v24, v0
	v_mov_b32_e32 v25, v0
	v_mov_b32_e32 v26, v0
	v_mov_b32_e32 v27, v0
	v_mov_b32_e32 v28, v0
	v_mov_b32_e32 v29, v0
	v_mov_b32_e32 v30, v0
	v_mov_b32_e32 v31, v0
	v_mov_b32_e32 v32, v0
	v_mov_b32_e32 v33, v0
	v_mov_b32_e32 v34, v0
	v_mov_b32_e32 v35, v0
	v_mov_b32_e32 v36, v0
	v_mov_b32_e32 v37, v0
	v_mov_b32_e32 v38, v0
	v_mov_b32_e32 v39, v0
	v_mov_b32_e32 v44, v0
	v_mov_b32_e32 v45, v0
	v_mov_b32_e32 v46, v0
	v_mov_b32_e32 v47, v0
	v_mov_b32_e32 v40, v0
	v_mov_b32_e32 v41, v0
	v_mov_b32_e32 v42, v0
	v_mov_b32_e32 v43, v0
	s_add_u32 s30, s22, s28
	s_addc_u32 s31, s23, s29
	s_add_u32 s30, s30, 0x180
	s_addc_u32 s31, s31, 0
	s_add_u32 s66, s24, s28
	s_addc_u32 s67, s25, s29
	s_add_u32 s68, s66, 0x180
	s_addc_u32 s69, s67, 0
	s_cmp_eq_u32 s60, s65
	s_cselect_b32 s67, s27, s31
	s_cselect_b32 s66, s26, s30
	s_cselect_b32 s31, s5, s69
	s_cselect_b32 s30, s4, s68
	s_add_i32 s68, s62, s42
	v_add_u32_e32 v131, 0, v128
	v_add_u32_e32 v182, 0, v127
	v_lshl_add_u64 v[180:181], v[116:117], 0, s[28:29]
.LBB6_22:
	s_mov_b32 m0, s68
	ds_read_b128 v[132:135], v131 offset:16384
	ds_read_b128 v[136:139], v131 offset:17408
	ds_read_b128 v[140:143], v131 offset:18432
	ds_read_b128 v[144:147], v131 offset:19456
	ds_read_b128 v[148:151], v182
	ds_read_b128 v[152:155], v182 offset:1024
	ds_read_b128 v[156:159], v182 offset:2048
	ds_read_b128 v[160:163], v182 offset:3072
	ds_read_b128 v[164:167], v182 offset:4096
	ds_read_b128 v[168:171], v182 offset:5120
	ds_read_b128 v[172:175], v182 offset:6144
	ds_read_b128 v[176:179], v182 offset:7168
	global_load_lds_dwordx4 v[180:181], off
	v_lshl_add_u64 v[180:181], v[118:119], 0, s[28:29]
	s_add_i32 m0, s68, 0x2000
	s_nop 0
	global_load_lds_dwordx4 v[180:181], off
	s_barrier
	s_waitcnt lgkmcnt(0)
	s_setprio 1
	s_waitcnt lgkmcnt(0)
	v_mfma_f32_16x16x32_f16 v[40:43], v[132:135], v[148:151], v[40:43]
	v_mfma_f32_16x16x32_f16 v[44:47], v[140:143], v[148:151], v[44:47]
	v_mfma_f32_16x16x32_f16 v[32:35], v[132:135], v[156:159], v[32:35]
	v_mfma_f32_16x16x32_f16 v[28:31], v[140:143], v[156:159], v[28:31]
	v_mfma_f32_16x16x32_f16 v[20:23], v[132:135], v[164:167], v[20:23]
	v_mfma_f32_16x16x32_f16 v[16:19], v[140:143], v[164:167], v[16:19]
	v_mfma_f32_16x16x32_f16 v[8:11], v[132:135], v[172:175], v[8:11]
	v_mfma_f32_16x16x32_f16 v[4:7], v[140:143], v[172:175], v[4:7]
	v_mfma_f32_16x16x32_f16 v[40:43], v[136:139], v[152:155], v[40:43]
	v_mfma_f32_16x16x32_f16 v[44:47], v[144:147], v[152:155], v[44:47]
	v_mfma_f32_16x16x32_f16 v[32:35], v[136:139], v[160:163], v[32:35]
	v_mfma_f32_16x16x32_f16 v[28:31], v[144:147], v[160:163], v[28:31]
	v_mfma_f32_16x16x32_f16 v[20:23], v[136:139], v[168:171], v[20:23]
	v_mfma_f32_16x16x32_f16 v[16:19], v[144:147], v[168:171], v[16:19]
	v_mfma_f32_16x16x32_f16 v[8:11], v[136:139], v[176:179], v[8:11]
	v_mfma_f32_16x16x32_f16 v[4:7], v[144:147], v[176:179], v[4:7]
	s_setprio 0
	s_barrier
	v_lshl_add_u64 v[140:141], v[120:121], 0, s[28:29]
	s_add_i32 m0, s47, 0x18000
	ds_read_b128 v[132:135], v131 offset:20480
	ds_read_b128 v[136:139], v131 offset:21504
	global_load_lds_dwordx4 v[140:141], off
	v_lshl_add_u64 v[140:141], v[122:123], 0, s[28:29]
	s_add_i32 m0, s47, 0x1a000
	s_nop 0
	global_load_lds_dwordx4 v[140:141], off
	v_lshl_add_u64 v[140:141], v[124:125], 0, s[28:29]
	s_add_i32 m0, s47, 0x1c000
	s_nop 0
	global_load_lds_dwordx4 v[140:141], off
	s_cmp_lg_u32 s65, 0
	s_cbranch_scc1 .Lm2_norm_0
	s_mul_i32 s70, s58, 0xc0
	v_add_u32_e32 v234, s70, v129
	v_ashrrev_i32_e32 v235, 31, v234
	v_lshlrev_b64 v[234:235], 2, v[234:235]
	v_lshl_add_u64 v[234:235], s[18:19], 0, v[234:235]
	global_load_dwordx4 v[222:225], v[234:235], off
	global_load_dwordx4 v[226:229], v[234:235], off offset:64
	global_load_dwordx4 v[230:233], v[234:235], off offset:128
	global_load_dwordx2 v[198:199], v[190:191], off
	global_load_dwordx2 v[200:201], v[190:191], off offset:32
	global_load_dwordx2 v[202:203], v[190:191], off offset:64
	global_load_dwordx2 v[204:205], v[192:193], off
	s_waitcnt vmcnt(12)
	s_branch .Lm2_join_0

.Lm2_join_2:
	s_barrier
	s_waitcnt lgkmcnt(0)
	s_setprio 1
	s_waitcnt lgkmcnt(0)
	v_mfma_f32_16x16x32_f16 v[36:39], v[132:135], v[148:151], v[36:39]
	v_mfma_f32_16x16x32_f16 v[24:27], v[132:135], v[156:159], v[24:27]
	v_mfma_f32_16x16x32_f16 v[12:15], v[132:135], v[164:167], v[12:15]
	v_mfma_f32_16x16x32_f16 v[0:3], v[132:135], v[172:175], v[0:3]
	v_mfma_f32_16x16x32_f16 v[36:39], v[136:139], v[152:155], v[36:39]
	v_mfma_f32_16x16x32_f16 v[24:27], v[136:139], v[160:163], v[24:27]
	v_mfma_f32_16x16x32_f16 v[12:15], v[136:139], v[168:171], v[12:15]
	v_mfma_f32_16x16x32_f16 v[0:3], v[136:139], v[176:179], v[0:3]
	s_setprio 0
	s_add_i32 s65, s65, 3
	s_add_u32 s28, s28, 0x180
	s_addc_u32 s29, s29, 0
	s_cmp_ge_i32 s65, s59
	s_cbranch_scc1 .Lrot_exit_mlp2
	s_add_u32 s30, s22, s28
	s_addc_u32 s31, s23, s29
	s_add_u32 s30, s30, 0x180
	s_addc_u32 s31, s31, 0
	s_add_u32 s66, s24, s28
	s_addc_u32 s67, s25, s29
	s_add_u32 s68, s66, 0x180
	s_addc_u32 s69, s67, 0
	s_cmp_eq_u32 s60, s65
	s_cselect_b32 s67, s27, s31
	s_cselect_b32 s66, s26, s30
	s_cselect_b32 s31, s5, s69
	s_cselect_b32 s30, s4, s68
	s_add_i32 s68, s62, s42
	v_add_u32_e32 v131, 0, v128
	v_add_u32_e32 v182, 0, v127
	v_lshl_add_u64 v[180:181], v[116:117], 0, s[28:29]
	s_barrier
	s_branch .LBB6_22
